# speedup vs baseline: 1.0136x; 1.0136x over previous
.LBB4_80:
	v_lshlrev_b64 v[6:7], 9, v[168:169]
	v_or_b32_e32 v6, v6, v198
	v_lshl_add_u64 v[2:3], s[20:21], 0, v[6:7]
	global_load_dwordx4 v[2:5], v[2:3], off
	v_lshl_add_u64 v[6:7], s[22:23], 0, v[6:7]
	global_load_dwordx4 v[6:9], v[6:7], off
	v_add_u32_e32 v168, v185, v199
	v_lshlrev_b64 v[26:27], 9, v[168:169]
	v_or_b32_e32 v26, v26, v198
	v_lshl_add_u64 v[22:23], s[20:21], 0, v[26:27]
	global_load_dwordx4 v[22:25], v[22:23], off
	v_lshl_add_u64 v[26:27], s[22:23], 0, v[26:27]
	global_load_dwordx4 v[26:29], v[26:27], off
	v_pk_add_f16 v17, v17, v33
	v_pk_add_f16 v16, v16, v32
	v_pk_add_f16 v15, v15, v31
	v_pk_add_f16 v14, v14, v30
	v_pk_fma_f16 v42, v13, v33, v21
	v_pk_fma_f16 v43, v12, v32, v20
	v_rcp_f16_e32 v12, v14
	v_rcp_f16_sdwa v13, v14 dst_sel:DWORD dst_unused:UNUSED_PAD src0_sel:WORD_1
	v_rcp_f16_e32 v14, v15
	v_rcp_f16_sdwa v15, v15 dst_sel:DWORD dst_unused:UNUSED_PAD src0_sel:WORD_1
	v_rcp_f16_e32 v46, v16
	v_rcp_f16_sdwa v16, v16 dst_sel:DWORD dst_unused:UNUSED_PAD src0_sel:WORD_1
	v_rcp_f16_e32 v47, v17
	v_rcp_f16_sdwa v17, v17 dst_sel:DWORD dst_unused:UNUSED_PAD src0_sel:WORD_1
	v_add_u32_e32 v168, v187, v199
	v_pk_fma_f16 v44, v10, v30, v18
	v_pk_fma_f16 v45, v11, v31, v19
	v_lshlrev_b64 v[10:11], 9, v[168:169]
	v_or_b32_e32 v10, v10, v198
	v_lshl_add_u64 v[38:39], s[20:21], 0, v[10:11]
	v_lshl_add_u64 v[40:41], s[22:23], 0, v[10:11]
	v_pack_b32_f16 v48, v14, v15
	v_pack_b32_f16 v49, v12, v13
	v_pack_b32_f16 v46, v46, v16
	v_pack_b32_f16 v47, v47, v17
	global_load_dwordx4 v[10:13], v[38:39], off
	global_load_dwordx4 v[14:17], v[40:41], off
	v_cvt_f32_f16_sdwa v21, v139 dst_sel:DWORD dst_unused:UNUSED_PAD src0_sel:WORD_1
	v_cvt_f32_f16_e32 v20, v139
	v_cvt_f32_f16_sdwa v19, v138 dst_sel:DWORD dst_unused:UNUSED_PAD src0_sel:WORD_1
	v_cvt_f32_f16_e32 v18, v138
	v_cvt_f32_f16_sdwa v33, v141 dst_sel:DWORD dst_unused:UNUSED_PAD src0_sel:WORD_1
	v_cvt_f32_f16_e32 v32, v141
	v_pk_mul_f16 v58, v43, v46
	v_pk_mul_f16 v59, v42, v47
	v_cvt_f32_f16_sdwa v31, v140 dst_sel:DWORD dst_unused:UNUSED_PAD src0_sel:WORD_1
	v_cvt_f32_f16_e32 v30, v140
	v_pk_mul_f16 v52, v45, v48
	v_pk_mul_f16 v53, v44, v49
	v_add_u32_e32 v168, v190, v199
	v_lshlrev_b64 v[36:37], 9, v[168:169]
	v_or_b32_e32 v36, v36, v198
	v_lshl_or_b32 v50, s46, 6, v178
	v_lshlrev_b32_e32 v51, 9, v50
	v_add_u32_e32 v203, v184, v51
	v_cvt_f32_f16_sdwa v35, v77 dst_sel:DWORD dst_unused:UNUSED_PAD src0_sel:WORD_1
	v_cvt_f32_f16_e32 v34, v77
	v_add_lshl_u32 v202, v188, v50, 9
	s_mov_b64 s[4:5], -1
	s_and_b64 vcc, exec, s[26:27]
	s_waitcnt vmcnt(5)
	v_cvt_f32_f16_e32 v38, v2
	v_cvt_f32_f16_sdwa v39, v2 dst_sel:DWORD dst_unused:UNUSED_PAD src0_sel:WORD_1
	v_cvt_f32_f16_e32 v2, v3
	v_cvt_f32_f16_sdwa v3, v3 dst_sel:DWORD dst_unused:UNUSED_PAD src0_sel:WORD_1
	s_waitcnt vmcnt(4)
	v_cvt_f32_f16_e32 v40, v6
	v_cvt_f32_f16_sdwa v41, v6 dst_sel:DWORD dst_unused:UNUSED_PAD src0_sel:WORD_1
	v_cvt_f32_f16_e32 v6, v7
	v_cvt_f32_f16_sdwa v7, v7 dst_sel:DWORD dst_unused:UNUSED_PAD src0_sel:WORD_1
	v_cvt_f32_f16_e32 v42, v4
	v_cvt_f32_f16_sdwa v43, v4 dst_sel:DWORD dst_unused:UNUSED_PAD src0_sel:WORD_1
	v_cvt_f32_f16_e32 v4, v5
	v_cvt_f32_f16_sdwa v5, v5 dst_sel:DWORD dst_unused:UNUSED_PAD src0_sel:WORD_1
	v_cvt_f32_f16_e32 v44, v8
	v_cvt_f32_f16_sdwa v45, v8 dst_sel:DWORD dst_unused:UNUSED_PAD src0_sel:WORD_1
	v_cvt_f32_f16_e32 v8, v9
	v_cvt_f32_f16_sdwa v9, v9 dst_sel:DWORD dst_unused:UNUSED_PAD src0_sel:WORD_1
	v_pk_add_f32 v[2:3], v[20:21], v[2:3]
	v_pk_add_f32 v[18:19], v[18:19], v[38:39]
	v_pk_add_f32 v[4:5], v[32:33], v[4:5]
	v_pk_add_f32 v[6:7], v[2:3], v[6:7]
	v_pk_add_f32 v[20:21], v[30:31], v[42:43]
	v_pk_add_f32 v[18:19], v[18:19], v[40:41]
	v_pk_add_f32 v[8:9], v[4:5], v[8:9]
	v_cvt_pk_f16_f32 v3, v6, v7
	v_lshl_add_u64 v[6:7], s[20:21], 0, v[36:37]
	v_pk_add_f32 v[20:21], v[20:21], v[44:45]
	v_cvt_pk_f16_f32 v2, v18, v19
	v_cvt_pk_f16_f32 v5, v8, v9
	global_load_dwordx4 v[6:9], v[6:7], off
	v_lshl_add_u64 v[18:19], s[22:23], 0, v[36:37]
	v_cvt_pk_f16_f32 v4, v20, v21
	global_load_dwordx4 v[18:21], v[18:19], off
	s_waitcnt vmcnt(5)
	v_cvt_f32_f16_e32 v46, v22
	v_cvt_f32_f16_sdwa v47, v22 dst_sel:DWORD dst_unused:UNUSED_PAD src0_sel:WORD_1
	ds_write_b128 v203, v[2:5]
	v_cvt_f32_f16_sdwa v5, v76 dst_sel:DWORD dst_unused:UNUSED_PAD src0_sel:WORD_1
	v_cvt_f32_f16_e32 v4, v76
	v_cvt_f32_f16_e32 v22, v23
	v_cvt_f32_f16_sdwa v23, v23 dst_sel:DWORD dst_unused:UNUSED_PAD src0_sel:WORD_1
	s_waitcnt vmcnt(4)
	v_cvt_f32_f16_e32 v48, v26
	v_cvt_f32_f16_sdwa v49, v26 dst_sel:DWORD dst_unused:UNUSED_PAD src0_sel:WORD_1
	v_cvt_f32_f16_e32 v26, v27
	v_cvt_f32_f16_sdwa v27, v27 dst_sel:DWORD dst_unused:UNUSED_PAD src0_sel:WORD_1
	v_cvt_f32_f16_sdwa v31, v75 dst_sel:DWORD dst_unused:UNUSED_PAD src0_sel:WORD_1
	v_cvt_f32_f16_e32 v30, v75
	v_cvt_f32_f16_e32 v32, v24
	v_cvt_f32_f16_sdwa v33, v24 dst_sel:DWORD dst_unused:UNUSED_PAD src0_sel:WORD_1
	v_pk_add_f32 v[4:5], v[4:5], v[22:23]
	v_cvt_f32_f16_e32 v22, v28
	v_pk_add_f32 v[4:5], v[4:5], v[26:27]
	v_cvt_f32_f16_sdwa v23, v28 dst_sel:DWORD dst_unused:UNUSED_PAD src0_sel:WORD_1
	v_cvt_f32_f16_sdwa v27, v74 dst_sel:DWORD dst_unused:UNUSED_PAD src0_sel:WORD_1
	v_cvt_f32_f16_e32 v26, v74
	v_cvt_f32_f16_e32 v24, v25
	v_cvt_f32_f16_sdwa v25, v25 dst_sel:DWORD dst_unused:UNUSED_PAD src0_sel:WORD_1
	v_pk_add_f32 v[2:3], v[34:35], v[46:47]
	v_cvt_f32_f16_e32 v28, v29
	v_cvt_f32_f16_sdwa v29, v29 dst_sel:DWORD dst_unused:UNUSED_PAD src0_sel:WORD_1
	v_pk_add_f32 v[2:3], v[2:3], v[48:49]
	s_nop 0
	v_cvt_pk_f16_f32 v2, v2, v3
	v_cvt_pk_f16_f32 v3, v4, v5
	v_pk_add_f32 v[4:5], v[30:31], v[32:33]
	s_nop 0
	v_pk_add_f32 v[4:5], v[4:5], v[22:23]
	v_pk_add_f32 v[22:23], v[26:27], v[24:25]
	v_cvt_pk_f16_f32 v4, v4, v5
	v_pk_add_f32 v[22:23], v[22:23], v[28:29]
	s_waitcnt vmcnt(3)
	v_cvt_f32_f16_e32 v24, v10
	v_cvt_pk_f16_f32 v5, v22, v23
	v_add_u32_e32 v22, v186, v50
	v_lshlrev_b32_e32 v204, 9, v22
	v_bitop3_b32 v22, v22, v179, 15 bitop3:0x6c
	v_lshlrev_b32_e32 v205, 4, v22
	v_cvt_f32_f16_sdwa v25, v10 dst_sel:DWORD dst_unused:UNUSED_PAD src0_sel:WORD_1
	v_or_b32_e32 v10, v205, v204
	v_cvt_f32_f16_sdwa v23, v57 dst_sel:DWORD dst_unused:UNUSED_PAD src0_sel:WORD_1
	v_cvt_f32_f16_e32 v22, v57
	ds_write_b128 v10, v[2:5]
	v_cvt_f32_f16_sdwa v5, v56 dst_sel:DWORD dst_unused:UNUSED_PAD src0_sel:WORD_1
	v_cvt_f32_f16_e32 v4, v56
	v_cvt_f32_f16_e32 v10, v11
	v_cvt_f32_f16_sdwa v11, v11 dst_sel:DWORD dst_unused:UNUSED_PAD src0_sel:WORD_1
	s_waitcnt vmcnt(2)
	v_cvt_f32_f16_e32 v26, v14
	v_cvt_f32_f16_sdwa v27, v14 dst_sel:DWORD dst_unused:UNUSED_PAD src0_sel:WORD_1
	v_cvt_f32_f16_e32 v14, v15
	v_cvt_f32_f16_sdwa v15, v15 dst_sel:DWORD dst_unused:UNUSED_PAD src0_sel:WORD_1
	v_pk_add_f32 v[2:3], v[22:23], v[24:25]
	v_cvt_f32_f16_sdwa v23, v55 dst_sel:DWORD dst_unused:UNUSED_PAD src0_sel:WORD_1
	v_cvt_f32_f16_e32 v22, v55
	v_cvt_f32_f16_e32 v24, v12
	v_cvt_f32_f16_sdwa v25, v12 dst_sel:DWORD dst_unused:UNUSED_PAD src0_sel:WORD_1
	v_pk_add_f32 v[4:5], v[4:5], v[10:11]
	v_cvt_f32_f16_e32 v10, v16
	v_pk_add_f32 v[4:5], v[4:5], v[14:15]
	v_cvt_f32_f16_sdwa v11, v16 dst_sel:DWORD dst_unused:UNUSED_PAD src0_sel:WORD_1
	v_cvt_f32_f16_sdwa v15, v54 dst_sel:DWORD dst_unused:UNUSED_PAD src0_sel:WORD_1
	v_cvt_f32_f16_e32 v14, v54
	v_cvt_f32_f16_e32 v12, v13
	v_cvt_f32_f16_sdwa v13, v13 dst_sel:DWORD dst_unused:UNUSED_PAD src0_sel:WORD_1
	v_cvt_f32_f16_e32 v16, v17
	v_cvt_f32_f16_sdwa v17, v17 dst_sel:DWORD dst_unused:UNUSED_PAD src0_sel:WORD_1
	v_pk_add_f32 v[2:3], v[2:3], v[26:27]
	s_nop 0
	v_cvt_pk_f16_f32 v2, v2, v3
	v_cvt_pk_f16_f32 v3, v4, v5
	v_pk_add_f32 v[4:5], v[22:23], v[24:25]
	s_nop 0
	v_pk_add_f32 v[4:5], v[4:5], v[10:11]
	v_pk_add_f32 v[10:11], v[14:15], v[12:13]
	v_cvt_pk_f16_f32 v4, v4, v5
	v_pk_add_f32 v[10:11], v[10:11], v[16:17]
	s_waitcnt vmcnt(1)
	v_cvt_f32_f16_e32 v12, v6
	v_cvt_pk_f16_f32 v5, v10, v11
	v_cvt_f32_f16_e32 v10, v53
	v_cvt_f32_f16_sdwa v11, v53 dst_sel:DWORD dst_unused:UNUSED_PAD src0_sel:WORD_1
	v_cvt_f32_f16_sdwa v13, v6 dst_sel:DWORD dst_unused:UNUSED_PAD src0_sel:WORD_1
	s_waitcnt vmcnt(0)
	v_cvt_f32_f16_e32 v14, v18
	v_cvt_f32_f16_sdwa v15, v18 dst_sel:DWORD dst_unused:UNUSED_PAD src0_sel:WORD_1
	v_or_b32_e32 v6, v189, v202
	ds_write_b128 v6, v[2:5]
	v_cvt_f32_f16_e32 v4, v52
	v_cvt_f32_f16_sdwa v5, v52 dst_sel:DWORD dst_unused:UNUSED_PAD src0_sel:WORD_1
	v_cvt_f32_f16_e32 v6, v7
	v_cvt_f32_f16_sdwa v7, v7 dst_sel:DWORD dst_unused:UNUSED_PAD src0_sel:WORD_1
	v_pk_add_f32 v[2:3], v[10:11], v[12:13]
	v_cvt_f32_f16_e32 v10, v19
	v_cvt_f32_f16_sdwa v11, v19 dst_sel:DWORD dst_unused:UNUSED_PAD src0_sel:WORD_1
	v_pk_add_f32 v[2:3], v[2:3], v[14:15]
	v_cvt_f32_f16_e32 v12, v58
	v_cvt_f32_f16_sdwa v13, v58 dst_sel:DWORD dst_unused:UNUSED_PAD src0_sel:WORD_1
	v_cvt_f32_f16_e32 v14, v8
	v_cvt_f32_f16_sdwa v15, v8 dst_sel:DWORD dst_unused:UNUSED_PAD src0_sel:WORD_1
	v_pk_add_f32 v[4:5], v[4:5], v[6:7]
	v_cvt_f32_f16_e32 v6, v20
	v_pk_add_f32 v[4:5], v[4:5], v[10:11]
	v_cvt_f32_f16_sdwa v7, v20 dst_sel:DWORD dst_unused:UNUSED_PAD src0_sel:WORD_1
	v_cvt_f32_f16_e32 v10, v59
	v_cvt_f32_f16_sdwa v11, v59 dst_sel:DWORD dst_unused:UNUSED_PAD src0_sel:WORD_1
	v_cvt_f32_f16_e32 v8, v9
	v_cvt_f32_f16_sdwa v9, v9 dst_sel:DWORD dst_unused:UNUSED_PAD src0_sel:WORD_1
	v_cvt_pk_f16_f32 v2, v2, v3
	v_cvt_pk_f16_f32 v3, v4, v5
	v_pk_add_f32 v[4:5], v[12:13], v[14:15]
	v_cvt_f32_f16_e32 v12, v21
	v_cvt_f32_f16_sdwa v13, v21 dst_sel:DWORD dst_unused:UNUSED_PAD src0_sel:WORD_1
	v_pk_add_f32 v[4:5], v[4:5], v[6:7]
	v_pk_add_f32 v[6:7], v[10:11], v[8:9]
	v_cvt_pk_f16_f32 v4, v4, v5
	v_pk_add_f32 v[6:7], v[6:7], v[12:13]
	s_nop 0
	v_cvt_pk_f16_f32 v5, v6, v7
	v_add_lshl_u32 v6, v191, v50, 9
	v_add_u32_e32 v168, v192, v6
	ds_write_b128 v168, v[2:5]
	global_load_dwordx4 v[2:5], v[174:175], off
	global_load_dwordx4 v[8:11], v[176:177], off
	global_load_dwordx4 v[12:15], v[174:175], off offset:16
	global_load_dwordx4 v[16:19], v[176:177], off offset:16
	s_cbranch_vccz .LBB4_118
	global_load_dwordx3 v[154:156], v169, s[18:19]
	s_mov_b32 s14, s38
	s_mov_b32 s15, s39
	v_cmp_lt_u32_e64 s[64:65], 0, v199
	v_cmp_gt_u32_e64 s[66:67], 63, v199
	v_cmp_lt_u32_e64 s[68:69], 0, v180
	v_cmp_gt_u32_e64 s[70:71], 60, v180
	buffer_load_dwordx4 v[210:213], v200, s[12:15], 0 offen
	s_and_b64 s[72:73], s[68:69], s[64:65]
	s_and_b64 s[74:75], s[68:69], s[66:67]
	s_and_b64 s[76:77], s[70:71], s[64:65]
	s_and_b64 s[78:79], s[70:71], s[66:67]
	v_add_u32_e32 v245, 0xfffe7c00, v200
	v_add_u32_e32 v246, 0xfffe8000, v200
	s_mov_b64 exec, s[72:73]
	buffer_load_dwordx4 v[122:125], v245, s[12:15], 0 offen
	buffer_load_dwordx4 v[82:85], v245, s[12:15], 0 offen offset:512
	s_mov_b64 exec, -1
	s_mov_b64 exec, s[68:69]
	buffer_load_dwordx4 v[138:141], v246, s[12:15], 0 offen offset:512
	buffer_load_dwordx4 v[106:109], v246, s[12:15], 0 offen offset:1024
	s_mov_b64 exec, -1
	s_mov_b64 exec, s[74:75]
	buffer_load_dwordx4 v[146:149], v246, s[12:15], 0 offen offset:2048
	buffer_load_dwordx4 v[126:129], v246, s[12:15], 0 offen offset:2560
	s_mov_b64 exec, -1
	v_add_u32_e32 v245, 0xfffffc00, v200
	s_mov_b64 exec, s[64:65]
	buffer_load_dwordx4 v[94:97], v245, s[12:15], 0 offen
	buffer_load_dwordx4 v[54:57], v245, s[12:15], 0 offen offset:512
	s_mov_b64 exec, -1
	buffer_load_dwordx4 v[118:121], v200, s[12:15], 0 offen offset:512
	buffer_load_dwordx4 v[74:77], v200, s[12:15], 0 offen offset:1024
	s_mov_b64 exec, s[66:67]
	buffer_load_dwordx4 v[134:137], v200, s[12:15], 0 offen offset:2048
	buffer_load_dwordx4 v[98:101], v200, s[12:15], 0 offen offset:2560
	s_mov_b64 exec, -1
	v_add_u32_e32 v245, 0x17c00, v200
	v_add_u32_e32 v246, 0x18000, v200
	s_mov_b64 exec, s[64:65]
	buffer_load_dwordx4 v[62:65], v245, s[12:15], 0 offen
	buffer_load_dwordx4 v[30:33], v245, s[12:15], 0 offen offset:512
	s_mov_b64 exec, -1
	buffer_load_dwordx4 v[78:81], v246, s[12:15], 0 offen offset:512
	buffer_load_dwordx4 v[42:45], v246, s[12:15], 0 offen offset:1024
	s_mov_b64 exec, s[66:67]
	buffer_load_dwordx4 v[102:105], v246, s[12:15], 0 offen offset:2048
	buffer_load_dwordx4 v[58:61], v246, s[12:15], 0 offen offset:2560
	s_mov_b64 exec, -1
	v_add_u32_e32 v245, 0x18000, v200
	buffer_load_dwordx4 v[162:165], v245, s[12:15], 0 offen
	v_add_u32_e32 v246, 0x30000, v200
	buffer_load_dwordx4 v[158:161], v246, s[12:15], 0 offen
	v_add_u32_e32 v245, 0x2fc00, v200
	v_add_u32_e32 v246, 0x30000, v200
	v_add_u32_e32 v247, 0x47c00, v200
	v_add_u32_e32 v248, 0x48000, v200
	v_add_u32_e32 v249, 0x5fc00, v200
	v_add_u32_e32 v250, 0x60000, v200
	s_waitcnt vmcnt(22)
	v_cvt_pk_f16_f32 v6, v2, v3
	v_cvt_pk_f16_f32 v2, v8, v9
	v_cvt_pk_f16_f32 v7, v4, v5
	v_cvt_pk_f16_f32 v3, v10, v11
	v_cvt_pk_f16_f32 v8, v12, v13
	v_cvt_pk_f16_f32 v4, v16, v17
	v_cvt_pk_f16_f32 v9, v14, v15
	v_cvt_pk_f16_f32 v5, v18, v19
	s_not_b64 exec, s[72:73]
	s_cbranch_execz .Lmyf_C3_0
	v_mov_b32_e32 v122, v6
	v_mov_b32_e32 v123, v7
	v_mov_b32_e32 v124, v8
	v_mov_b32_e32 v125, v9
	v_mov_b32_e32 v82, v2
	v_mov_b32_e32 v83, v3
	v_mov_b32_e32 v84, v4
	v_mov_b32_e32 v85, v5

_Z7k_attn2ILi2EEv8AttnArgs:
	v_readfirstlane_b32 s3, v0
	s_lshl_b32 s12, s3, 1
	v_lshlrev_b32_e32 v3, 3, v0
	s_and_b32 s12, s12, 0x80
	v_and_b32_e32 v3, 0x78, v3
	s_load_dwordx4 s[8:11], s[0:1], 0x0
	s_load_dwordx2 s[4:5], s[0:1], 0x10
	s_load_dwordx2 s[6:7], s[0:1], 0x50
	v_or_b32_e32 v180, s12, v3
	s_lshl_b32 s12, s2, 5
	v_lshrrev_b32_e32 v1, 5, v0
	v_bfe_u32 v2, v0, 4, 2
	s_and_b32 s14, s12, 0xe0
	s_lshr_b32 s12, s2, 3
	v_lshrrev_b32_e32 v0, 6, v0
	v_and_b32_e32 v1, 4, v1
	s_add_i32 s14, s14, s12
	s_and_b32 s2, s2, 56
	v_and_b32_e32 v0, 4, v0
	v_and_or_b32 v181, s14, 56, v0
	v_or3_b32 v182, v2, s2, v1
	s_and_b32 s2, s14, 0x3ffffc0
	v_or_b32_e32 v4, s2, v181
	v_lshlrev_b32_e32 v0, 1, v180
	v_mov_b32_e32 v1, 0
	s_waitcnt lgkmcnt(0)
	v_lshl_add_u64 v[2:3], s[6:7], 0, v[0:1]
	v_lshl_or_b32 v0, v4, 6, v182
	v_lshlrev_b64 v[4:5], 9, v[0:1]
	v_lshl_add_u64 v[8:9], v[2:3], 0, v[4:5]
	v_or_b32_e32 v4, 64, v0
	v_mov_b32_e32 v5, v1
	v_lshlrev_b64 v[4:5], 9, v[4:5]
	v_lshlrev_b32_e32 v20, 2, v180
	v_lshl_add_u64 v[10:11], v[2:3], 0, v[4:5]
	global_load_dwordx4 v[240:243], v20, s[10:11] offset:16
	global_load_dwordx4 v[236:239], v20, s[10:11]
	global_load_dwordx4 v[248:251], v20, s[4:5] offset:16
	global_load_dwordx4 v[244:247], v20, s[4:5]
	global_load_dwordx4 v[12:15], v[8:9], off
	global_load_dwordx4 v[4:7], v[10:11], off
	v_or_b32_e32 v8, 0x80, v0
	v_mov_b32_e32 v9, v1
	v_lshlrev_b64 v[8:9], 9, v[8:9]
	v_or_b32_e32 v0, 0xc0, v0
	v_lshl_add_u64 v[20:21], v[2:3], 0, v[8:9]
	v_lshlrev_b64 v[0:1], 9, v[0:1]
	v_lshl_add_u64 v[34:35], v[2:3], 0, v[0:1]
	global_load_dwordx4 v[8:11], v[20:21], off
	global_load_dwordx4 v[0:3], v[34:35], off
	s_bitcmp1_b32 s3, 6
	s_cselect_b64 s[4:5], -1, 0
	s_and_b32 s2, s14, 0x3ffc0
	v_or_b32_e32 v20, s2, v181
	v_lshl_or_b32 v20, v20, 6, v182
	v_add_u32_e32 v184, -1, v182
	v_add_u32_e32 v185, -1, v181
	v_mul_u32_u24_e32 v20, 0x300, v20
	v_or_b32_e32 v34, v185, v184
	v_or_b32_e32 v20, v180, v20
	s_mov_b32 s11, 0x20000
	s_mov_b32 s10, 0x1800000
	s_and_b32 s9, s9, 0xffff
	v_lshlrev_b32_e32 v183, 1, v20
	v_cmp_gt_u32_e64 s[2:3], 64, v34
	s_and_b64 vcc, exec, s[4:5]
	s_cbranch_vccz .LBB6_38
	s_load_dwordx2 s[12:13], s[0:1], 0x20
	s_waitcnt lgkmcnt(0)
	s_load_dwordx2 s[4:5], s[12:13], 0x0
	s_load_dword s12, s[12:13], 0x8
	v_cmp_lt_u32_e64 s[64:65], 0, v182
	v_cmp_gt_u32_e64 s[66:67], 63, v182
	v_cmp_lt_u32_e64 s[68:69], 0, v181
	v_cmp_gt_u32_e64 s[70:71], 60, v181
	buffer_load_dwordx4 v[190:193], v183, s[8:11], 0 offen
	s_and_b64 s[72:73], s[68:69], s[64:65]
	s_and_b64 s[74:75], s[68:69], s[66:67]
	s_and_b64 s[76:77], s[70:71], s[64:65]
	s_and_b64 s[78:79], s[70:71], s[66:67]
	v_add_u32_e32 v228, 0xfffe7c00, v183
	v_add_u32_e32 v229, 0xfffe8000, v183
	s_mov_b64 exec, s[72:73]
	buffer_load_dwordx4 v[136:139], v228, s[8:11], 0 offen
	buffer_load_dwordx4 v[96:99], v228, s[8:11], 0 offen offset:512
	s_mov_b64 exec, -1
	s_mov_b64 exec, s[68:69]
	buffer_load_dwordx4 v[152:155], v229, s[8:11], 0 offen offset:512
	buffer_load_dwordx4 v[124:127], v229, s[8:11], 0 offen offset:1024
	s_mov_b64 exec, -1
	s_mov_b64 exec, s[74:75]
	buffer_load_dwordx4 v[160:163], v229, s[8:11], 0 offen offset:2048
	buffer_load_dwordx4 v[140:143], v229, s[8:11], 0 offen offset:2560
	s_mov_b64 exec, -1
	v_add_u32_e32 v228, 0xfffffc00, v183
	s_mov_b64 exec, s[64:65]
	buffer_load_dwordx4 v[112:115], v228, s[8:11], 0 offen
	buffer_load_dwordx4 v[68:71], v228, s[8:11], 0 offen offset:512
	s_mov_b64 exec, -1
	buffer_load_dwordx4 v[132:135], v183, s[8:11], 0 offen offset:512
	buffer_load_dwordx4 v[88:91], v183, s[8:11], 0 offen offset:1024
	s_mov_b64 exec, s[66:67]
	buffer_load_dwordx4 v[148:151], v183, s[8:11], 0 offen offset:2048
	buffer_load_dwordx4 v[108:111], v183, s[8:11], 0 offen offset:2560
	s_mov_b64 exec, -1
	v_add_u32_e32 v228, 0x17c00, v183
	v_add_u32_e32 v229, 0x18000, v183
	s_mov_b64 exec, s[64:65]
	buffer_load_dwordx4 v[76:79], v228, s[8:11], 0 offen
	buffer_load_dwordx4 v[48:51], v228, s[8:11], 0 offen offset:512
	s_mov_b64 exec, -1
	buffer_load_dwordx4 v[92:95], v229, s[8:11], 0 offen offset:512
	buffer_load_dwordx4 v[56:59], v229, s[8:11], 0 offen offset:1024
	s_mov_b64 exec, s[66:67]
	buffer_load_dwordx4 v[116:119], v229, s[8:11], 0 offen offset:2048
	buffer_load_dwordx4 v[72:75], v229, s[8:11], 0 offen offset:2560
	s_mov_b64 exec, -1
	v_add_u32_e32 v228, 0x18000, v183
	buffer_load_dwordx4 v[176:179], v228, s[8:11], 0 offen
	v_add_u32_e32 v229, 0x30000, v183
	buffer_load_dwordx4 v[172:175], v229, s[8:11], 0 offen
	v_add_u32_e32 v228, 0x48000, v183
	buffer_load_dwordx4 v[168:171], v228, s[8:11], 0 offen
	v_add_u32_e32 v228, 0x2fc00, v183
	v_add_u32_e32 v229, 0x30000, v183
	v_add_u32_e32 v230, 0x47c00, v183
	v_add_u32_e32 v231, 0x48000, v183
	v_add_u32_e32 v232, 0x5fc00, v183
	v_add_u32_e32 v233, 0x60000, v183
	s_waitcnt vmcnt(26)
	v_cvt_pk_f16_f32 v22, v240, v241
	v_cvt_pk_f16_f32 v20, v236, v237
	v_cvt_pk_f16_f32 v21, v238, v239
	v_cvt_pk_f16_f32 v16, v244, v245
	v_cvt_pk_f16_f32 v17, v246, v247
	v_cvt_pk_f16_f32 v18, v248, v249
	v_cvt_pk_f16_f32 v23, v242, v243
	v_cvt_pk_f16_f32 v19, v250, v251
	s_not_b64 exec, s[72:73]
	s_cbranch_execz .Lmyf_E1_0
	v_mov_b32_e32 v136, v20
	v_mov_b32_e32 v137, v21
	v_mov_b32_e32 v138, v22
	v_mov_b32_e32 v139, v23
	v_mov_b32_e32 v96, v16
	v_mov_b32_e32 v97, v17
	v_mov_b32_e32 v98, v18
	v_mov_b32_e32 v99, v19
